# v34 + P4 attention-group combine: all 4 token rows' loads issued up front (was one exposed load latency per row)
# baseline (speedup 1.0000x reference)
.LBB0_876:
	v_lshl_add_u64 v[14:15], s[50:51], 0, v[12:13]
	v_mov_b64_e32 v[146:147], v[14:15]
	v_add_co_u32_e64 v30, s[0:1], s10, v14
	v_lshl_add_u64 v[16:17], s[50:51], 0, v[10:11]
	s_nop 0
	v_addc_co_u32_e64 v31, s[0:1], 0, v15, s[0:1]
	v_add_co_u32_e64 v28, s[0:1], s11, v14
	v_add_co_u32_e32 v26, vcc, 0x200000, v16
	s_nop 0
	v_addc_co_u32_e64 v29, s[0:1], 0, v15, s[0:1]
	v_add_co_u32_e64 v32, s[0:1], s12, v14
	v_addc_co_u32_e32 v27, vcc, 0, v17, vcc
	s_nop 0
	v_addc_co_u32_e64 v33, s[0:1], 0, v15, s[0:1]
	global_load_dwordx4 v[130:133], v[28:29], off
	global_load_dwordx4 v[134:137], v[32:33], off
	v_add_co_u32_e32 v32, vcc, 0x240000, v16
	global_load_dword v142, v[26:27], off
	s_nop 0
	v_addc_co_u32_e32 v33, vcc, 0, v17, vcc
	v_add_co_u32_e32 v16, vcc, 0x280000, v16
	s_nop 0
	s_nop 0
	v_addc_co_u32_e32 v17, vcc, 0, v17, vcc
	global_load_dword v143, v[32:33], off
	global_load_dword v144, v[16:17], off
	global_load_dwordx4 v[138:141], v[30:31], off
	s_nop 0
	s_nop 0
	s_nop 0
	v_lshl_add_u64 v[12:13], v[12:13], 0, s[8:9]
	v_lshl_add_u64 v[10:11], v[10:11], 0, 32
	v_lshl_add_u64 v[14:15], s[50:51], 0, v[12:13]
	v_mov_b64_e32 v[164:165], v[14:15]
	v_add_co_u32_e64 v30, s[0:1], s10, v14
	v_lshl_add_u64 v[16:17], s[50:51], 0, v[10:11]
	s_nop 0
	v_addc_co_u32_e64 v31, s[0:1], 0, v15, s[0:1]
	v_add_co_u32_e64 v28, s[0:1], s11, v14
	v_add_co_u32_e32 v26, vcc, 0x200000, v16
	s_nop 0
	v_addc_co_u32_e64 v29, s[0:1], 0, v15, s[0:1]
	v_add_co_u32_e64 v32, s[0:1], s12, v14
	v_addc_co_u32_e32 v27, vcc, 0, v17, vcc
	s_nop 0
	v_addc_co_u32_e64 v33, s[0:1], 0, v15, s[0:1]
	global_load_dwordx4 v[148:151], v[28:29], off
	global_load_dwordx4 v[152:155], v[32:33], off
	v_add_co_u32_e32 v32, vcc, 0x240000, v16
	global_load_dword v160, v[26:27], off
	s_nop 0
	v_addc_co_u32_e32 v33, vcc, 0, v17, vcc
	v_add_co_u32_e32 v16, vcc, 0x280000, v16
	s_nop 0
	s_nop 0
	v_addc_co_u32_e32 v17, vcc, 0, v17, vcc
	global_load_dword v161, v[32:33], off
	global_load_dword v162, v[16:17], off
	global_load_dwordx4 v[156:159], v[30:31], off
	s_nop 0
	s_nop 0
	s_nop 0
	v_lshl_add_u64 v[12:13], v[12:13], 0, s[8:9]
	v_lshl_add_u64 v[10:11], v[10:11], 0, 32
	v_lshl_add_u64 v[14:15], s[50:51], 0, v[12:13]
	v_mov_b64_e32 v[186:187], v[14:15]
	v_add_co_u32_e64 v30, s[0:1], s10, v14
	v_lshl_add_u64 v[16:17], s[50:51], 0, v[10:11]
	s_nop 0
	v_addc_co_u32_e64 v31, s[0:1], 0, v15, s[0:1]
	v_add_co_u32_e64 v28, s[0:1], s11, v14
	v_add_co_u32_e32 v26, vcc, 0x200000, v16
	s_nop 0
	v_addc_co_u32_e64 v29, s[0:1], 0, v15, s[0:1]
	v_add_co_u32_e64 v32, s[0:1], s12, v14
	v_addc_co_u32_e32 v27, vcc, 0, v17, vcc
	s_nop 0
	v_addc_co_u32_e64 v33, s[0:1], 0, v15, s[0:1]
	global_load_dwordx4 v[166:169], v[28:29], off
	global_load_dwordx4 v[170:173], v[32:33], off
	v_add_co_u32_e32 v32, vcc, 0x240000, v16
	global_load_dword v183, v[26:27], off
	s_nop 0
	v_addc_co_u32_e32 v33, vcc, 0, v17, vcc
	v_add_co_u32_e32 v16, vcc, 0x280000, v16
	s_nop 0
	s_nop 0
	v_addc_co_u32_e32 v17, vcc, 0, v17, vcc
	global_load_dword v184, v[32:33], off
	global_load_dword v185, v[16:17], off
	global_load_dwordx4 v[174:177], v[30:31], off
	s_nop 0
	s_nop 0
	s_nop 0
	v_lshl_add_u64 v[12:13], v[12:13], 0, s[8:9]
	v_lshl_add_u64 v[10:11], v[10:11], 0, 32
	v_lshl_add_u64 v[14:15], s[50:51], 0, v[12:13]
	v_mov_b64_e32 v[224:225], v[14:15]
	v_add_co_u32_e64 v30, s[0:1], s10, v14
	v_lshl_add_u64 v[16:17], s[50:51], 0, v[10:11]
	s_nop 0
	v_addc_co_u32_e64 v31, s[0:1], 0, v15, s[0:1]
	v_add_co_u32_e64 v28, s[0:1], s11, v14
	v_add_co_u32_e32 v26, vcc, 0x200000, v16
	s_nop 0
	v_addc_co_u32_e64 v29, s[0:1], 0, v15, s[0:1]
	v_add_co_u32_e64 v32, s[0:1], s12, v14
	v_addc_co_u32_e32 v27, vcc, 0, v17, vcc
	s_nop 0
	v_addc_co_u32_e64 v33, s[0:1], 0, v15, s[0:1]
	global_load_dwordx4 v[188:191], v[28:29], off
	global_load_dwordx4 v[198:201], v[32:33], off
	v_add_co_u32_e32 v32, vcc, 0x240000, v16
	global_load_dword v192, v[26:27], off
	s_nop 0
	v_addc_co_u32_e32 v33, vcc, 0, v17, vcc
	v_add_co_u32_e32 v16, vcc, 0x280000, v16
	s_nop 0
	s_nop 0
	v_addc_co_u32_e32 v17, vcc, 0, v17, vcc
	global_load_dword v193, v[32:33], off
	global_load_dword v202, v[16:17], off
	global_load_dwordx4 v[220:223], v[30:31], off
	s_nop 0
	s_nop 0
	s_nop 0
	v_lshl_add_u64 v[12:13], v[12:13], 0, s[8:9]
	v_lshl_add_u64 v[10:11], v[10:11], 0, 32
	s_waitcnt vmcnt(18)
	v_mov_b32_e32 v18, v130
	v_mov_b32_e32 v19, v131
	v_mov_b32_e32 v20, v132
	v_mov_b32_e32 v21, v133
	v_mov_b32_e32 v22, v134
	v_mov_b32_e32 v23, v135
	v_mov_b32_e32 v24, v136
	v_mov_b32_e32 v25, v137
	v_mov_b32_e32 v26, v138
	v_mov_b32_e32 v27, v139
	v_mov_b32_e32 v28, v140
	v_mov_b32_e32 v29, v141
	v_mov_b32_e32 v64, v142
	v_mov_b32_e32 v65, v143
	v_mov_b32_e32 v66, v144
	v_mov_b64_e32 v[14:15], v[146:147]
	v_mov_b32_e32 v2, 0
	v_mov_b32_e32 v3, 0
	v_mov_b32_e32 v4, 0
	v_mov_b32_e32 v5, 0
	v_cvt_pk_f32_fp8_e32 v[16:17], v18
	v_cvt_pk_f32_fp8_e32 v[32:33], v22
	v_cvt_pk_f32_fp8_sdwa v[34:35], v22 src0_sel:WORD_1
	v_cvt_pk_f32_fp8_e32 v[38:39], v23
	v_cvt_pk_f32_fp8_sdwa v[22:23], v23 src0_sel:WORD_1
	v_cvt_pk_f32_fp8_e32 v[44:45], v24
	v_cvt_pk_f32_fp8_sdwa v[46:47], v24 src0_sel:WORD_1
	v_cvt_pk_f32_fp8_e32 v[50:51], v25
	v_cvt_pk_f32_fp8_sdwa v[24:25], v25 src0_sel:WORD_1
	v_mov_b32_e32 v71, v22
	v_cvt_pk_f32_fp8_sdwa v[30:31], v18 src0_sel:WORD_1
	v_max3_f32 v67, v64, v65, v66
	v_sub_f32_e32 v68, v64, v67
	v_sub_f32_e32 v65, v65, v67
	v_sub_f32_e32 v66, v66, v67
	v_mov_b32_e32 v79, v24
	v_mul_f32_e32 v22, 0x3fb8aa3b, v68
	v_mul_f32_e32 v24, 0x3fb8aa3b, v65
	v_cvt_pk_f32_fp8_e32 v[52:53], v26
	v_cvt_pk_f32_fp8_sdwa v[54:55], v26 src0_sel:WORD_1
	v_cvt_pk_f32_fp8_e32 v[56:57], v27
	v_cvt_pk_f32_fp8_sdwa v[26:27], v27 src0_sel:WORD_1
	v_mov_b32_e32 v67, v34
	v_mul_f32_e32 v34, 0x3fb8aa3b, v66
	v_exp_f32_e32 v80, v22
	v_exp_f32_e32 v65, v24
	v_exp_f32_e32 v81, v34
	v_cvt_pk_f32_fp8_e32 v[58:59], v28
	v_cvt_pk_f32_fp8_sdwa v[60:61], v28 src0_sel:WORD_1
	v_cvt_pk_f32_fp8_e32 v[62:63], v29
	v_cvt_pk_f32_fp8_sdwa v[28:29], v29 src0_sel:WORD_1
	v_mov_b32_e32 v70, v26
	v_add_f32_e32 v26, v80, v65
	v_add_f32_e32 v26, v81, v26
	v_mov_b32_e32 v22, v27
	v_div_scale_f32 v27, s[0:1], v26, v26, 1.0
	v_mov_b32_e32 v24, v29
	v_rcp_f32_e32 v29, v27
	v_mov_b32_e32 v66, v54
	v_mov_b32_e32 v78, v28
	v_div_scale_f32 v28, vcc, 1.0, v26, 1.0
	v_fma_f32 v54, -v27, v29, 1.0
	v_fmac_f32_e32 v29, v54, v29
	v_mul_f32_e32 v54, v28, v29
	v_mov_b32_e32 v34, v55
	v_fma_f32 v55, -v27, v54, v28
	v_fmac_f32_e32 v54, v55, v29
	v_fma_f32 v27, -v27, v54, v28
	v_div_fmas_f32 v27, v27, v29, v54
	v_cvt_pk_f32_fp8_e32 v[36:37], v19
	v_cvt_pk_f32_fp8_sdwa v[18:19], v19 src0_sel:WORD_1
	v_cvt_pk_f32_fp8_e32 v[40:41], v20
	v_cvt_pk_f32_fp8_sdwa v[42:43], v20 src0_sel:WORD_1
	v_cvt_pk_f32_fp8_e32 v[48:49], v21
	v_div_fixup_f32 v26, v27, v26, 1.0
	v_cvt_pk_f32_fp8_sdwa v[20:21], v21 src0_sel:WORD_1
	v_mul_f32_e32 v82, v65, v26
	v_pk_mul_f32 v[26:27], v[80:81], v[26:27] op_sel_hi:[1,0]
	v_mov_b32_e32 v64, v32
	v_mov_b32_e32 v69, v38
	v_mov_b32_e32 v73, v44
	v_mov_b32_e32 v75, v46
	v_mov_b32_e32 v77, v50
	v_mov_b32_e32 v68, v56
	v_mov_b32_e32 v38, v57
	v_mov_b32_e32 v72, v58
	v_mov_b32_e32 v44, v59
	v_mov_b32_e32 v74, v60
	v_mov_b32_e32 v46, v61
	v_mov_b32_e32 v76, v62
	v_mov_b32_e32 v50, v63
	v_pk_mov_b32 v[28:29], v[26:27], v[52:53] op_sel:[1,0]
	v_mov_b32_e32 v65, v26
	v_mov_b32_e32 v52, v27
	v_pk_mov_b32 v[32:33], v[32:33], v[26:27] op_sel:[1,0]
	v_pk_mul_f32 v[54:55], v[26:27], v[66:67]
	v_pk_mul_f32 v[34:35], v[26:27], v[34:35]
	v_pk_mul_f32 v[56:57], v[26:27], v[68:69]
	v_pk_mul_f32 v[38:39], v[26:27], v[38:39]
	v_pk_mul_f32 v[58:59], v[26:27], v[70:71]
	v_pk_mul_f32 v[22:23], v[26:27], v[22:23]
	v_pk_mul_f32 v[60:61], v[26:27], v[72:73]
	v_pk_mul_f32 v[44:45], v[26:27], v[44:45]
	v_pk_mul_f32 v[62:63], v[26:27], v[74:75]
	v_pk_mul_f32 v[46:47], v[26:27], v[46:47]
	v_pk_mul_f32 v[66:67], v[26:27], v[76:77]
	v_pk_mul_f32 v[50:51], v[26:27], v[50:51]
	v_pk_mul_f32 v[68:69], v[26:27], v[78:79]
	v_pk_mul_f32 v[24:25], v[26:27], v[24:25]
	v_pk_mul_f32 v[26:27], v[28:29], v[64:65]
	v_pk_mul_f32 v[28:29], v[52:53], v[32:33]
	v_fma_f32 v30, v30, v82, v54
	v_fma_f32 v31, v31, v82, v34
	v_fma_f32 v32, v82, v36, v56
	v_fma_f32 v33, v82, v37, v38
	v_fma_f32 v19, v82, v19, v22
	v_fma_f32 v22, v82, v40, v60
	v_fma_f32 v34, v82, v41, v44
	v_fma_f32 v36, v82, v42, v62
	v_fma_f32 v38, v82, v48, v66
	v_fma_f32 v40, v82, v49, v50
	v_fma_f32 v16, v16, v82, v27
	v_fma_f32 v17, v17, v82, v29
	v_fma_f32 v21, v82, v21, v24
	v_add_f32_e32 v24, v30, v55
	v_add_f32_e32 v27, v31, v35
	v_add_f32_e32 v29, v32, v57
	v_add_f32_e32 v30, v33, v39
	v_add_f32_e32 v19, v19, v23
	v_add_f32_e32 v22, v22, v61
	v_add_f32_e32 v23, v34, v45
	v_add_f32_e32 v31, v36, v63
	v_add_f32_e32 v33, v38, v67
	v_add_f32_e32 v34, v40, v51
	v_add_f32_e32 v16, v26, v16
	v_add_f32_e32 v17, v28, v17
	v_add_f32_e32 v21, v21, v25
	v_med3_f32 v25, v27, s13, v1
	v_med3_f32 v26, v29, s13, v1
	v_med3_f32 v27, v30, s13, v1
	v_med3_f32 v22, v22, s13, v1
	v_med3_f32 v23, v23, s13, v1
	v_med3_f32 v28, v31, s13, v1
	v_med3_f32 v30, v33, s13, v1
	v_med3_f32 v31, v34, s13, v1
	v_med3_f32 v16, v16, s13, v1
	v_med3_f32 v17, v17, s13, v1
	v_cvt_pk_fp8_f32 v3, v26, v27
	v_cvt_pk_fp8_f32 v4, v22, v23
	v_cvt_pk_fp8_f32 v5, v30, v31
	v_cvt_pk_fp8_f32 v2, v16, v17
	v_fma_f32 v18, v82, v18, v58
	v_fma_f32 v37, v82, v43, v46
	v_fma_f32 v20, v82, v20, v68
	v_add_f32_e32 v18, v18, v59
	v_add_f32_e32 v32, v37, v47
	v_add_f32_e32 v20, v20, v69
	v_med3_f32 v24, v24, s13, v1
	v_med3_f32 v18, v18, s13, v1
	v_med3_f32 v19, v19, s13, v1
	v_med3_f32 v29, v32, s13, v1
	v_med3_f32 v20, v20, s13, v1
	v_med3_f32 v21, v21, s13, v1
	v_cvt_pk_fp8_f32 v3, v18, v19 op_sel:[0,0,1]
	v_cvt_pk_fp8_f32 v4, v28, v29 op_sel:[0,0,1]
	v_cvt_pk_fp8_f32 v5, v20, v21 op_sel:[0,0,1]
	v_cvt_pk_fp8_f32 v2, v24, v25 op_sel:[0,0,1]
	v_add_co_u32_e32 v14, vcc, 0x25600000, v14
	s_nop 1
	v_addc_co_u32_e32 v15, vcc, 0, v15, vcc
	global_store_dwordx4 v[14:15], v[2:5], off
	s_waitcnt vmcnt(12)
	v_mov_b32_e32 v18, v148
	v_mov_b32_e32 v19, v149
	v_mov_b32_e32 v20, v150
	v_mov_b32_e32 v21, v151
	v_mov_b32_e32 v22, v152
	v_mov_b32_e32 v23, v153
	v_mov_b32_e32 v24, v154
	v_mov_b32_e32 v25, v155
	v_mov_b32_e32 v26, v156
	v_mov_b32_e32 v27, v157
	v_mov_b32_e32 v28, v158
	v_mov_b32_e32 v29, v159
	v_mov_b32_e32 v64, v160
	v_mov_b32_e32 v65, v161
	v_mov_b32_e32 v66, v162
	v_mov_b64_e32 v[14:15], v[164:165]
	v_mov_b32_e32 v2, 0
	v_mov_b32_e32 v3, 0
	v_mov_b32_e32 v4, 0
	v_mov_b32_e32 v5, 0
	v_cvt_pk_f32_fp8_e32 v[16:17], v18
	v_cvt_pk_f32_fp8_e32 v[32:33], v22
	v_cvt_pk_f32_fp8_sdwa v[34:35], v22 src0_sel:WORD_1
	v_cvt_pk_f32_fp8_e32 v[38:39], v23
	v_cvt_pk_f32_fp8_sdwa v[22:23], v23 src0_sel:WORD_1
	v_cvt_pk_f32_fp8_e32 v[44:45], v24
	v_cvt_pk_f32_fp8_sdwa v[46:47], v24 src0_sel:WORD_1
	v_cvt_pk_f32_fp8_e32 v[50:51], v25
	v_cvt_pk_f32_fp8_sdwa v[24:25], v25 src0_sel:WORD_1
	v_mov_b32_e32 v71, v22
	v_cvt_pk_f32_fp8_sdwa v[30:31], v18 src0_sel:WORD_1
	v_max3_f32 v67, v64, v65, v66
	v_sub_f32_e32 v68, v64, v67
	v_sub_f32_e32 v65, v65, v67
	v_sub_f32_e32 v66, v66, v67
	v_mov_b32_e32 v79, v24
	v_mul_f32_e32 v22, 0x3fb8aa3b, v68
	v_mul_f32_e32 v24, 0x3fb8aa3b, v65
	v_cvt_pk_f32_fp8_e32 v[52:53], v26
	v_cvt_pk_f32_fp8_sdwa v[54:55], v26 src0_sel:WORD_1
	v_cvt_pk_f32_fp8_e32 v[56:57], v27
	v_cvt_pk_f32_fp8_sdwa v[26:27], v27 src0_sel:WORD_1
	v_mov_b32_e32 v67, v34
	v_mul_f32_e32 v34, 0x3fb8aa3b, v66
	v_exp_f32_e32 v80, v22
	v_exp_f32_e32 v65, v24
	v_exp_f32_e32 v81, v34
	v_cvt_pk_f32_fp8_e32 v[58:59], v28
	v_cvt_pk_f32_fp8_sdwa v[60:61], v28 src0_sel:WORD_1
	v_cvt_pk_f32_fp8_e32 v[62:63], v29
	v_cvt_pk_f32_fp8_sdwa v[28:29], v29 src0_sel:WORD_1
	v_mov_b32_e32 v70, v26
	v_add_f32_e32 v26, v80, v65
	v_add_f32_e32 v26, v81, v26
	v_mov_b32_e32 v22, v27
	v_div_scale_f32 v27, s[0:1], v26, v26, 1.0
	v_mov_b32_e32 v24, v29
	v_rcp_f32_e32 v29, v27
	v_mov_b32_e32 v66, v54
	v_mov_b32_e32 v78, v28
	v_div_scale_f32 v28, vcc, 1.0, v26, 1.0
	v_fma_f32 v54, -v27, v29, 1.0
	v_fmac_f32_e32 v29, v54, v29
	v_mul_f32_e32 v54, v28, v29
	v_mov_b32_e32 v34, v55
	v_fma_f32 v55, -v27, v54, v28
	v_fmac_f32_e32 v54, v55, v29
	v_fma_f32 v27, -v27, v54, v28
	v_div_fmas_f32 v27, v27, v29, v54
	v_cvt_pk_f32_fp8_e32 v[36:37], v19
	v_cvt_pk_f32_fp8_sdwa v[18:19], v19 src0_sel:WORD_1
	v_cvt_pk_f32_fp8_e32 v[40:41], v20
	v_cvt_pk_f32_fp8_sdwa v[42:43], v20 src0_sel:WORD_1
	v_cvt_pk_f32_fp8_e32 v[48:49], v21
	v_div_fixup_f32 v26, v27, v26, 1.0
	v_cvt_pk_f32_fp8_sdwa v[20:21], v21 src0_sel:WORD_1
	v_mul_f32_e32 v82, v65, v26
	v_pk_mul_f32 v[26:27], v[80:81], v[26:27] op_sel_hi:[1,0]
	v_mov_b32_e32 v64, v32
	v_mov_b32_e32 v69, v38
	v_mov_b32_e32 v73, v44
	v_mov_b32_e32 v75, v46
	v_mov_b32_e32 v77, v50
	v_mov_b32_e32 v68, v56
	v_mov_b32_e32 v38, v57
	v_mov_b32_e32 v72, v58
	v_mov_b32_e32 v44, v59
	v_mov_b32_e32 v74, v60
	v_mov_b32_e32 v46, v61
	v_mov_b32_e32 v76, v62
	v_mov_b32_e32 v50, v63
	v_pk_mov_b32 v[28:29], v[26:27], v[52:53] op_sel:[1,0]
	v_mov_b32_e32 v65, v26
	v_mov_b32_e32 v52, v27
	v_pk_mov_b32 v[32:33], v[32:33], v[26:27] op_sel:[1,0]
	v_pk_mul_f32 v[54:55], v[26:27], v[66:67]
	v_pk_mul_f32 v[34:35], v[26:27], v[34:35]
	v_pk_mul_f32 v[56:57], v[26:27], v[68:69]
	v_pk_mul_f32 v[38:39], v[26:27], v[38:39]
	v_pk_mul_f32 v[58:59], v[26:27], v[70:71]
	v_pk_mul_f32 v[22:23], v[26:27], v[22:23]
	v_pk_mul_f32 v[60:61], v[26:27], v[72:73]
	v_pk_mul_f32 v[44:45], v[26:27], v[44:45]
	v_pk_mul_f32 v[62:63], v[26:27], v[74:75]
	v_pk_mul_f32 v[46:47], v[26:27], v[46:47]
	v_pk_mul_f32 v[66:67], v[26:27], v[76:77]
	v_pk_mul_f32 v[50:51], v[26:27], v[50:51]
	v_pk_mul_f32 v[68:69], v[26:27], v[78:79]
	v_pk_mul_f32 v[24:25], v[26:27], v[24:25]
	v_pk_mul_f32 v[26:27], v[28:29], v[64:65]
	v_pk_mul_f32 v[28:29], v[52:53], v[32:33]
	v_fma_f32 v30, v30, v82, v54
	v_fma_f32 v31, v31, v82, v34
	v_fma_f32 v32, v82, v36, v56
	v_fma_f32 v33, v82, v37, v38
	v_fma_f32 v19, v82, v19, v22
	v_fma_f32 v22, v82, v40, v60
	v_fma_f32 v34, v82, v41, v44
	v_fma_f32 v36, v82, v42, v62
	v_fma_f32 v38, v82, v48, v66
	v_fma_f32 v40, v82, v49, v50
	v_fma_f32 v16, v16, v82, v27
	v_fma_f32 v17, v17, v82, v29
	v_fma_f32 v21, v82, v21, v24
	v_add_f32_e32 v24, v30, v55
	v_add_f32_e32 v27, v31, v35
	v_add_f32_e32 v29, v32, v57
	v_add_f32_e32 v30, v33, v39
	v_add_f32_e32 v19, v19, v23
	v_add_f32_e32 v22, v22, v61
	v_add_f32_e32 v23, v34, v45
	v_add_f32_e32 v31, v36, v63
	v_add_f32_e32 v33, v38, v67
	v_add_f32_e32 v34, v40, v51
	v_add_f32_e32 v16, v26, v16
	v_add_f32_e32 v17, v28, v17
	v_add_f32_e32 v21, v21, v25
	v_med3_f32 v25, v27, s13, v1
	v_med3_f32 v26, v29, s13, v1
	v_med3_f32 v27, v30, s13, v1
	v_med3_f32 v22, v22, s13, v1
	v_med3_f32 v23, v23, s13, v1
	v_med3_f32 v28, v31, s13, v1
	v_med3_f32 v30, v33, s13, v1
	v_med3_f32 v31, v34, s13, v1
	v_med3_f32 v16, v16, s13, v1
	v_med3_f32 v17, v17, s13, v1
	v_cvt_pk_fp8_f32 v3, v26, v27
	v_cvt_pk_fp8_f32 v4, v22, v23
	v_cvt_pk_fp8_f32 v5, v30, v31
	v_cvt_pk_fp8_f32 v2, v16, v17
	v_fma_f32 v18, v82, v18, v58
	v_fma_f32 v37, v82, v43, v46
	v_fma_f32 v20, v82, v20, v68
	v_add_f32_e32 v18, v18, v59
	v_add_f32_e32 v32, v37, v47
	v_add_f32_e32 v20, v20, v69
	v_med3_f32 v24, v24, s13, v1
	v_med3_f32 v18, v18, s13, v1
	v_med3_f32 v19, v19, s13, v1
	v_med3_f32 v29, v32, s13, v1
	v_med3_f32 v20, v20, s13, v1
	v_med3_f32 v21, v21, s13, v1
	v_cvt_pk_fp8_f32 v3, v18, v19 op_sel:[0,0,1]
	v_cvt_pk_fp8_f32 v4, v28, v29 op_sel:[0,0,1]
	v_cvt_pk_fp8_f32 v5, v20, v21 op_sel:[0,0,1]
	v_cvt_pk_fp8_f32 v2, v24, v25 op_sel:[0,0,1]
	v_add_co_u32_e32 v14, vcc, 0x25600000, v14
	s_nop 1
	v_addc_co_u32_e32 v15, vcc, 0, v15, vcc
	global_store_dwordx4 v[14:15], v[2:5], off
	s_waitcnt vmcnt(6)
	v_mov_b32_e32 v18, v166
	v_mov_b32_e32 v19, v167
	v_mov_b32_e32 v20, v168
	v_mov_b32_e32 v21, v169
	v_mov_b32_e32 v22, v170
	v_mov_b32_e32 v23, v171
	v_mov_b32_e32 v24, v172
	v_mov_b32_e32 v25, v173
	v_mov_b32_e32 v26, v174
	v_mov_b32_e32 v27, v175
	v_mov_b32_e32 v28, v176
	v_mov_b32_e32 v29, v177
	v_mov_b32_e32 v64, v183
	v_mov_b32_e32 v65, v184
	v_mov_b32_e32 v66, v185
	v_mov_b64_e32 v[14:15], v[186:187]
	v_mov_b32_e32 v2, 0
	v_mov_b32_e32 v3, 0
	v_mov_b32_e32 v4, 0
	v_mov_b32_e32 v5, 0
	v_cvt_pk_f32_fp8_e32 v[16:17], v18
	v_cvt_pk_f32_fp8_e32 v[32:33], v22
	v_cvt_pk_f32_fp8_sdwa v[34:35], v22 src0_sel:WORD_1
	v_cvt_pk_f32_fp8_e32 v[38:39], v23
	v_cvt_pk_f32_fp8_sdwa v[22:23], v23 src0_sel:WORD_1
	v_cvt_pk_f32_fp8_e32 v[44:45], v24
	v_cvt_pk_f32_fp8_sdwa v[46:47], v24 src0_sel:WORD_1
	v_cvt_pk_f32_fp8_e32 v[50:51], v25
	v_cvt_pk_f32_fp8_sdwa v[24:25], v25 src0_sel:WORD_1
	v_mov_b32_e32 v71, v22
	v_cvt_pk_f32_fp8_sdwa v[30:31], v18 src0_sel:WORD_1
	v_max3_f32 v67, v64, v65, v66
	v_sub_f32_e32 v68, v64, v67
	v_sub_f32_e32 v65, v65, v67
	v_sub_f32_e32 v66, v66, v67
	v_mov_b32_e32 v79, v24
	v_mul_f32_e32 v22, 0x3fb8aa3b, v68
	v_mul_f32_e32 v24, 0x3fb8aa3b, v65
	v_cvt_pk_f32_fp8_e32 v[52:53], v26
	v_cvt_pk_f32_fp8_sdwa v[54:55], v26 src0_sel:WORD_1
	v_cvt_pk_f32_fp8_e32 v[56:57], v27
	v_cvt_pk_f32_fp8_sdwa v[26:27], v27 src0_sel:WORD_1
	v_mov_b32_e32 v67, v34
	v_mul_f32_e32 v34, 0x3fb8aa3b, v66
	v_exp_f32_e32 v80, v22
	v_exp_f32_e32 v65, v24
	v_exp_f32_e32 v81, v34
	v_cvt_pk_f32_fp8_e32 v[58:59], v28
	v_cvt_pk_f32_fp8_sdwa v[60:61], v28 src0_sel:WORD_1
	v_cvt_pk_f32_fp8_e32 v[62:63], v29
	v_cvt_pk_f32_fp8_sdwa v[28:29], v29 src0_sel:WORD_1
	v_mov_b32_e32 v70, v26
	v_add_f32_e32 v26, v80, v65
	v_add_f32_e32 v26, v81, v26
	v_mov_b32_e32 v22, v27
	v_div_scale_f32 v27, s[0:1], v26, v26, 1.0
	v_mov_b32_e32 v24, v29
	v_rcp_f32_e32 v29, v27
	v_mov_b32_e32 v66, v54
	v_mov_b32_e32 v78, v28
	v_div_scale_f32 v28, vcc, 1.0, v26, 1.0
	v_fma_f32 v54, -v27, v29, 1.0
	v_fmac_f32_e32 v29, v54, v29
	v_mul_f32_e32 v54, v28, v29
	v_mov_b32_e32 v34, v55
	v_fma_f32 v55, -v27, v54, v28
	v_fmac_f32_e32 v54, v55, v29
	v_fma_f32 v27, -v27, v54, v28
	v_div_fmas_f32 v27, v27, v29, v54
	v_cvt_pk_f32_fp8_e32 v[36:37], v19
	v_cvt_pk_f32_fp8_sdwa v[18:19], v19 src0_sel:WORD_1
	v_cvt_pk_f32_fp8_e32 v[40:41], v20
	v_cvt_pk_f32_fp8_sdwa v[42:43], v20 src0_sel:WORD_1
	v_cvt_pk_f32_fp8_e32 v[48:49], v21
	v_div_fixup_f32 v26, v27, v26, 1.0
	v_cvt_pk_f32_fp8_sdwa v[20:21], v21 src0_sel:WORD_1
	v_mul_f32_e32 v82, v65, v26
	v_pk_mul_f32 v[26:27], v[80:81], v[26:27] op_sel_hi:[1,0]
	v_mov_b32_e32 v64, v32
	v_mov_b32_e32 v69, v38
	v_mov_b32_e32 v73, v44
	v_mov_b32_e32 v75, v46
	v_mov_b32_e32 v77, v50
	v_mov_b32_e32 v68, v56
	v_mov_b32_e32 v38, v57
	v_mov_b32_e32 v72, v58
	v_mov_b32_e32 v44, v59
	v_mov_b32_e32 v74, v60
	v_mov_b32_e32 v46, v61
	v_mov_b32_e32 v76, v62
	v_mov_b32_e32 v50, v63
	v_pk_mov_b32 v[28:29], v[26:27], v[52:53] op_sel:[1,0]
	v_mov_b32_e32 v65, v26
	v_mov_b32_e32 v52, v27
	v_pk_mov_b32 v[32:33], v[32:33], v[26:27] op_sel:[1,0]
	v_pk_mul_f32 v[54:55], v[26:27], v[66:67]
	v_pk_mul_f32 v[34:35], v[26:27], v[34:35]
	v_pk_mul_f32 v[56:57], v[26:27], v[68:69]
	v_pk_mul_f32 v[38:39], v[26:27], v[38:39]
	v_pk_mul_f32 v[58:59], v[26:27], v[70:71]
	v_pk_mul_f32 v[22:23], v[26:27], v[22:23]
	v_pk_mul_f32 v[60:61], v[26:27], v[72:73]
	v_pk_mul_f32 v[44:45], v[26:27], v[44:45]
	v_pk_mul_f32 v[62:63], v[26:27], v[74:75]
	v_pk_mul_f32 v[46:47], v[26:27], v[46:47]
	v_pk_mul_f32 v[66:67], v[26:27], v[76:77]
	v_pk_mul_f32 v[50:51], v[26:27], v[50:51]
	v_pk_mul_f32 v[68:69], v[26:27], v[78:79]
	v_pk_mul_f32 v[24:25], v[26:27], v[24:25]
	v_pk_mul_f32 v[26:27], v[28:29], v[64:65]
	v_pk_mul_f32 v[28:29], v[52:53], v[32:33]
	v_fma_f32 v30, v30, v82, v54
	v_fma_f32 v31, v31, v82, v34
	v_fma_f32 v32, v82, v36, v56
	v_fma_f32 v33, v82, v37, v38
	v_fma_f32 v19, v82, v19, v22
	v_fma_f32 v22, v82, v40, v60
	v_fma_f32 v34, v82, v41, v44
	v_fma_f32 v36, v82, v42, v62
	v_fma_f32 v38, v82, v48, v66
	v_fma_f32 v40, v82, v49, v50
	v_fma_f32 v16, v16, v82, v27
	v_fma_f32 v17, v17, v82, v29
	v_fma_f32 v21, v82, v21, v24
	v_add_f32_e32 v24, v30, v55
	v_add_f32_e32 v27, v31, v35
	v_add_f32_e32 v29, v32, v57
	v_add_f32_e32 v30, v33, v39
	v_add_f32_e32 v19, v19, v23
	v_add_f32_e32 v22, v22, v61
	v_add_f32_e32 v23, v34, v45
	v_add_f32_e32 v31, v36, v63
	v_add_f32_e32 v33, v38, v67
	v_add_f32_e32 v34, v40, v51
	v_add_f32_e32 v16, v26, v16
	v_add_f32_e32 v17, v28, v17
	v_add_f32_e32 v21, v21, v25
	v_med3_f32 v25, v27, s13, v1
	v_med3_f32 v26, v29, s13, v1
	v_med3_f32 v27, v30, s13, v1
	v_med3_f32 v22, v22, s13, v1
	v_med3_f32 v23, v23, s13, v1
	v_med3_f32 v28, v31, s13, v1
	v_med3_f32 v30, v33, s13, v1
	v_med3_f32 v31, v34, s13, v1
	v_med3_f32 v16, v16, s13, v1
	v_med3_f32 v17, v17, s13, v1
	v_cvt_pk_fp8_f32 v3, v26, v27
	v_cvt_pk_fp8_f32 v4, v22, v23
	v_cvt_pk_fp8_f32 v5, v30, v31
	v_cvt_pk_fp8_f32 v2, v16, v17
	v_fma_f32 v18, v82, v18, v58
	v_fma_f32 v37, v82, v43, v46
	v_fma_f32 v20, v82, v20, v68
	v_add_f32_e32 v18, v18, v59
	v_add_f32_e32 v32, v37, v47
	v_add_f32_e32 v20, v20, v69
	v_med3_f32 v24, v24, s13, v1
	v_med3_f32 v18, v18, s13, v1
	v_med3_f32 v19, v19, s13, v1
	v_med3_f32 v29, v32, s13, v1
	v_med3_f32 v20, v20, s13, v1
	v_med3_f32 v21, v21, s13, v1
	v_cvt_pk_fp8_f32 v3, v18, v19 op_sel:[0,0,1]
	v_cvt_pk_fp8_f32 v4, v28, v29 op_sel:[0,0,1]
	v_cvt_pk_fp8_f32 v5, v20, v21 op_sel:[0,0,1]
	v_cvt_pk_fp8_f32 v2, v24, v25 op_sel:[0,0,1]
	v_add_co_u32_e32 v14, vcc, 0x25600000, v14
	s_nop 1
	v_addc_co_u32_e32 v15, vcc, 0, v15, vcc
	global_store_dwordx4 v[14:15], v[2:5], off
	s_waitcnt vmcnt(0)
	v_mov_b32_e32 v18, v188
	v_mov_b32_e32 v19, v189
	v_mov_b32_e32 v20, v190
	v_mov_b32_e32 v21, v191
	v_mov_b32_e32 v22, v198
	v_mov_b32_e32 v23, v199
	v_mov_b32_e32 v24, v200
	v_mov_b32_e32 v25, v201
	v_mov_b32_e32 v26, v220
	v_mov_b32_e32 v27, v221
	v_mov_b32_e32 v28, v222
	v_mov_b32_e32 v29, v223
	v_mov_b32_e32 v64, v192
	v_mov_b32_e32 v65, v193
	v_mov_b32_e32 v66, v202
	v_mov_b64_e32 v[14:15], v[224:225]
	v_mov_b32_e32 v2, 0
	v_mov_b32_e32 v3, 0
	v_mov_b32_e32 v4, 0
	v_mov_b32_e32 v5, 0
	v_cvt_pk_f32_fp8_e32 v[16:17], v18
	v_cvt_pk_f32_fp8_e32 v[32:33], v22
	v_cvt_pk_f32_fp8_sdwa v[34:35], v22 src0_sel:WORD_1
	v_cvt_pk_f32_fp8_e32 v[38:39], v23
	v_cvt_pk_f32_fp8_sdwa v[22:23], v23 src0_sel:WORD_1
	v_cvt_pk_f32_fp8_e32 v[44:45], v24
	v_cvt_pk_f32_fp8_sdwa v[46:47], v24 src0_sel:WORD_1
	v_cvt_pk_f32_fp8_e32 v[50:51], v25
	v_cvt_pk_f32_fp8_sdwa v[24:25], v25 src0_sel:WORD_1
	v_mov_b32_e32 v71, v22
	v_cvt_pk_f32_fp8_sdwa v[30:31], v18 src0_sel:WORD_1
	v_max3_f32 v67, v64, v65, v66
	v_sub_f32_e32 v68, v64, v67
	v_sub_f32_e32 v65, v65, v67
	v_sub_f32_e32 v66, v66, v67
	v_mov_b32_e32 v79, v24
	v_mul_f32_e32 v22, 0x3fb8aa3b, v68
	v_mul_f32_e32 v24, 0x3fb8aa3b, v65
	v_cvt_pk_f32_fp8_e32 v[52:53], v26
	v_cvt_pk_f32_fp8_sdwa v[54:55], v26 src0_sel:WORD_1
	v_cvt_pk_f32_fp8_e32 v[56:57], v27
	v_cvt_pk_f32_fp8_sdwa v[26:27], v27 src0_sel:WORD_1
	v_mov_b32_e32 v67, v34
	v_mul_f32_e32 v34, 0x3fb8aa3b, v66
	v_exp_f32_e32 v80, v22
	v_exp_f32_e32 v65, v24
	v_exp_f32_e32 v81, v34
	v_cvt_pk_f32_fp8_e32 v[58:59], v28
	v_cvt_pk_f32_fp8_sdwa v[60:61], v28 src0_sel:WORD_1
	v_cvt_pk_f32_fp8_e32 v[62:63], v29
	v_cvt_pk_f32_fp8_sdwa v[28:29], v29 src0_sel:WORD_1
	v_mov_b32_e32 v70, v26
	v_add_f32_e32 v26, v80, v65
	v_add_f32_e32 v26, v81, v26
	v_mov_b32_e32 v22, v27
	v_div_scale_f32 v27, s[0:1], v26, v26, 1.0
	v_mov_b32_e32 v24, v29
	v_rcp_f32_e32 v29, v27
	v_mov_b32_e32 v66, v54
	v_mov_b32_e32 v78, v28
	v_div_scale_f32 v28, vcc, 1.0, v26, 1.0
	v_fma_f32 v54, -v27, v29, 1.0
	v_fmac_f32_e32 v29, v54, v29
	v_mul_f32_e32 v54, v28, v29
	v_mov_b32_e32 v34, v55
	v_fma_f32 v55, -v27, v54, v28
	v_fmac_f32_e32 v54, v55, v29
	v_fma_f32 v27, -v27, v54, v28
	v_div_fmas_f32 v27, v27, v29, v54
	v_cvt_pk_f32_fp8_e32 v[36:37], v19
	v_cvt_pk_f32_fp8_sdwa v[18:19], v19 src0_sel:WORD_1
	v_cvt_pk_f32_fp8_e32 v[40:41], v20
	v_cvt_pk_f32_fp8_sdwa v[42:43], v20 src0_sel:WORD_1
	v_cvt_pk_f32_fp8_e32 v[48:49], v21
	v_div_fixup_f32 v26, v27, v26, 1.0
	v_cvt_pk_f32_fp8_sdwa v[20:21], v21 src0_sel:WORD_1
	v_mul_f32_e32 v82, v65, v26
	v_pk_mul_f32 v[26:27], v[80:81], v[26:27] op_sel_hi:[1,0]
	v_mov_b32_e32 v64, v32
	v_mov_b32_e32 v69, v38
	v_mov_b32_e32 v73, v44
	v_mov_b32_e32 v75, v46
	v_mov_b32_e32 v77, v50
	v_mov_b32_e32 v68, v56
	v_mov_b32_e32 v38, v57
	v_mov_b32_e32 v72, v58
	v_mov_b32_e32 v44, v59
	v_mov_b32_e32 v74, v60
	v_mov_b32_e32 v46, v61
	v_mov_b32_e32 v76, v62
	v_mov_b32_e32 v50, v63
	v_pk_mov_b32 v[28:29], v[26:27], v[52:53] op_sel:[1,0]
	v_mov_b32_e32 v65, v26
	v_mov_b32_e32 v52, v27
	v_pk_mov_b32 v[32:33], v[32:33], v[26:27] op_sel:[1,0]
	v_pk_mul_f32 v[54:55], v[26:27], v[66:67]
	v_pk_mul_f32 v[34:35], v[26:27], v[34:35]
	v_pk_mul_f32 v[56:57], v[26:27], v[68:69]
	v_pk_mul_f32 v[38:39], v[26:27], v[38:39]
	v_pk_mul_f32 v[58:59], v[26:27], v[70:71]
	v_pk_mul_f32 v[22:23], v[26:27], v[22:23]
	v_pk_mul_f32 v[60:61], v[26:27], v[72:73]
	v_pk_mul_f32 v[44:45], v[26:27], v[44:45]
	v_pk_mul_f32 v[62:63], v[26:27], v[74:75]
	v_pk_mul_f32 v[46:47], v[26:27], v[46:47]
	v_pk_mul_f32 v[66:67], v[26:27], v[76:77]
	v_pk_mul_f32 v[50:51], v[26:27], v[50:51]
	v_pk_mul_f32 v[68:69], v[26:27], v[78:79]
	v_pk_mul_f32 v[24:25], v[26:27], v[24:25]
	v_pk_mul_f32 v[26:27], v[28:29], v[64:65]
	v_pk_mul_f32 v[28:29], v[52:53], v[32:33]
	v_fma_f32 v30, v30, v82, v54
	v_fma_f32 v31, v31, v82, v34
	v_fma_f32 v32, v82, v36, v56
	v_fma_f32 v33, v82, v37, v38
	v_fma_f32 v19, v82, v19, v22
	v_fma_f32 v22, v82, v40, v60
	v_fma_f32 v34, v82, v41, v44
	v_fma_f32 v36, v82, v42, v62
	v_fma_f32 v38, v82, v48, v66
	v_fma_f32 v40, v82, v49, v50
	v_fma_f32 v16, v16, v82, v27
	v_fma_f32 v17, v17, v82, v29
	v_fma_f32 v21, v82, v21, v24
	v_add_f32_e32 v24, v30, v55
	v_add_f32_e32 v27, v31, v35
	v_add_f32_e32 v29, v32, v57
	v_add_f32_e32 v30, v33, v39
	v_add_f32_e32 v19, v19, v23
	v_add_f32_e32 v22, v22, v61
	v_add_f32_e32 v23, v34, v45
	v_add_f32_e32 v31, v36, v63
	v_add_f32_e32 v33, v38, v67
	v_add_f32_e32 v34, v40, v51
	v_add_f32_e32 v16, v26, v16
	v_add_f32_e32 v17, v28, v17
	v_add_f32_e32 v21, v21, v25
	v_med3_f32 v25, v27, s13, v1
	v_med3_f32 v26, v29, s13, v1
	v_med3_f32 v27, v30, s13, v1
	v_med3_f32 v22, v22, s13, v1
	v_med3_f32 v23, v23, s13, v1
	v_med3_f32 v28, v31, s13, v1
	v_med3_f32 v30, v33, s13, v1
	v_med3_f32 v31, v34, s13, v1
	v_med3_f32 v16, v16, s13, v1
	v_med3_f32 v17, v17, s13, v1
	v_cvt_pk_fp8_f32 v3, v26, v27
	v_cvt_pk_fp8_f32 v4, v22, v23
	v_cvt_pk_fp8_f32 v5, v30, v31
	v_cvt_pk_fp8_f32 v2, v16, v17
	v_fma_f32 v18, v82, v18, v58
	v_fma_f32 v37, v82, v43, v46
	v_fma_f32 v20, v82, v20, v68
	v_add_f32_e32 v18, v18, v59
	v_add_f32_e32 v32, v37, v47
	v_add_f32_e32 v20, v20, v69
	v_med3_f32 v24, v24, s13, v1
	v_med3_f32 v18, v18, s13, v1
	v_med3_f32 v19, v19, s13, v1
	v_med3_f32 v29, v32, s13, v1
	v_med3_f32 v20, v20, s13, v1
	v_med3_f32 v21, v21, s13, v1
	v_cvt_pk_fp8_f32 v3, v18, v19 op_sel:[0,0,1]
	v_cvt_pk_fp8_f32 v4, v28, v29 op_sel:[0,0,1]
	v_cvt_pk_fp8_f32 v5, v20, v21 op_sel:[0,0,1]
	v_cvt_pk_fp8_f32 v2, v24, v25 op_sel:[0,0,1]
	v_add_co_u32_e32 v14, vcc, 0x25600000, v14
	s_nop 1
	v_addc_co_u32_e32 v15, vcc, 0, v15, vcc
	global_store_dwordx4 v[14:15], v[2:5], off
	s_add_i32 s14, s14, s52
	v_lshl_add_u64 v[6:7], v[6:7], 0, s[4:5]
	s_cmpk_lt_i32 s14, 0x100
	v_lshl_add_u64 v[8:9], v[8:9], 0, s[6:7]
	s_cbranch_scc1 .LBB0_875
